# attention: last PV k-step of a tile issued at the start of the next tile's VALU segment (4 of 24 MFMAs leave the MFMA segment)
# baseline (speedup 1.0000x reference)
; #define LAS __attribute__((address_space(3)))
; __device__ __forceinline__ unsigned pk2(float lo, float hi) { f32x2_t v = {lo, hi}; bf16x2_t b = __builtin_convertvector(v, bf16x2_t); return __builtin_bit_cast(unsigned, b); }
; #define AT_STOREK(st) do { _Pragma("unroll") for (int i_ = 0; i_ < 2; ++i_) *(LAS u32x4*)(L + AT_K + (st) * AT_KBYTES + (prow0 + 32 * i_) * AT_KSTR + pch * 16) = kreg[i_]; } while (0)
; #define AT_STOREV(st) do { _Pragma("unroll") for (int i_ = 0; i_ < 2; ++i_) *(LAS u32x4*)(L + AT_V + (st) * AT_VBYTES + (prow0 + 32 * i_) * AT_VSTR + pch * 16) = vreg[i_]; } while (0)
; __device__ __forceinline__ void attn_unit(const Frame& F, int layer, int qrow0, int ntiles, int b, int head, float lam, float m2, float lam_init) {
;     ...
;         float ls = 0.f;
; #pragma unroll
;         for (int i = 0; i < 16; ++i) { sa[i] = __builtin_amdgcn_exp2f(sa[i]); sb[i] = __builtin_amdgcn_exp2f(sb[i]); ls += sa[i] + sb[i]; }
;         lsum += ls;
;         bf16x8 pk[4];
;         { u32x4 w0, w1, w2, w3;
; #pragma unroll
;           for (int i = 0; i < 4; ++i) { w0[i] = pk2(sa[2 * i], sa[2 * i + 1]); w1[i] = pk2(sa[8 + 2 * i], sa[9 + 2 * i]); w2[i] = pk2(sb[2 * i], sb[2 * i + 1]); w3[i] = pk2(sb[8 + 2 * i], sb[9 + 2 * i]); }
;           pk[0] = __builtin_bit_cast(bf16x8, w0); pk[1] = __builtin_bit_cast(bf16x8, w1); pk[2] = __builtin_bit_cast(bf16x8, w2); pk[3] = __builtin_bit_cast(bf16x8, w3); }
;         LAS const unsigned char* Vt = L + AT_V + (t & 1) * AT_VBYTES;
;     ...
;         if (t + 2 < ntiles) AT_STOREK(t & 1);
;         if (t + 1 < ntiles) AT_STOREV((t + 1) & 1);
;         __syncthreads();
;         sa = na; sb = nb;
.Latt_novload_it0:
	v_mfma_f32_32x32x16_bf16 v[32:47], v[180:183], v[218:221], v[32:47]
	v_mfma_f32_32x32x16_bf16 v[48:63], v[180:183], v[222:225], v[48:63]
	v_mfma_f32_32x32x16_bf16 v[0:15], v[180:183], v[226:229], v[0:15]
	v_mfma_f32_32x32x16_bf16 v[16:31], v[180:183], v[230:233], v[16:31]
	v_exp_f32_e32 v80, v80
	v_exp_f32_e32 v96, v96
	v_exp_f32_e32 v81, v81
	v_exp_f32_e32 v97, v97
	v_exp_f32_e32 v82, v82
	v_exp_f32_e32 v98, v98
	v_exp_f32_e32 v83, v83
	v_exp_f32_e32 v99, v99
	v_exp_f32_e32 v84, v84
	v_exp_f32_e32 v100, v100
	v_exp_f32_e32 v85, v85
	v_exp_f32_e32 v101, v101
	v_exp_f32_e32 v86, v86
	v_exp_f32_e32 v102, v102
	v_exp_f32_e32 v87, v87
	v_exp_f32_e32 v103, v103
	v_exp_f32_e32 v88, v88
	v_exp_f32_e32 v104, v104
	v_exp_f32_e32 v89, v89
	v_exp_f32_e32 v105, v105
	v_exp_f32_e32 v90, v90
	v_exp_f32_e32 v106, v106
	v_exp_f32_e32 v91, v91
	v_exp_f32_e32 v107, v107
	v_exp_f32_e32 v92, v92
	v_exp_f32_e32 v108, v108
	v_exp_f32_e32 v93, v93
	v_exp_f32_e32 v109, v109
	v_exp_f32_e32 v94, v94
	v_exp_f32_e32 v110, v110
	v_exp_f32_e32 v95, v95
	v_exp_f32_e32 v111, v111
	v_cvt_pk_bf16_f32 v112, v80, v81
	v_cvt_pk_bf16_f32 v113, v82, v83
	v_cvt_pk_bf16_f32 v114, v84, v85
	v_cvt_pk_bf16_f32 v115, v86, v87
	v_cvt_pk_bf16_f32 v116, v88, v89
	v_cvt_pk_bf16_f32 v117, v90, v91
	v_cvt_pk_bf16_f32 v118, v92, v93
	v_cvt_pk_bf16_f32 v119, v94, v95
	v_cvt_pk_bf16_f32 v120, v96, v97
	v_cvt_pk_bf16_f32 v121, v98, v99
	v_cvt_pk_bf16_f32 v122, v100, v101
	v_cvt_pk_bf16_f32 v123, v102, v103
	v_cvt_pk_bf16_f32 v124, v104, v105
	v_cvt_pk_bf16_f32 v125, v106, v107
	v_cvt_pk_bf16_f32 v126, v108, v109
	v_cvt_pk_bf16_f32 v127, v110, v111
	v_add_f32_e32 v80, v80, v96
	v_add_f32_e32 v81, v81, v97
	v_add_f32_e32 v82, v82, v98
	v_add_f32_e32 v83, v83, v99
	v_add_f32_e32 v84, v84, v100
	v_add_f32_e32 v85, v85, v101
	v_add_f32_e32 v86, v86, v102
	v_add_f32_e32 v87, v87, v103
	v_add_f32_e32 v88, v88, v104
	v_add_f32_e32 v89, v89, v105
	v_add_f32_e32 v90, v90, v106
	v_add_f32_e32 v91, v91, v107
	v_add_f32_e32 v92, v92, v108
	v_add_f32_e32 v93, v93, v109
	v_add_f32_e32 v94, v94, v110
	v_add_f32_e32 v95, v95, v111
	v_add_f32_e32 v80, v80, v88
	v_add_f32_e32 v81, v81, v89
	v_add_f32_e32 v82, v82, v90
	v_add_f32_e32 v83, v83, v91
	v_add_f32_e32 v84, v84, v92
	v_add_f32_e32 v85, v85, v93
	v_add_f32_e32 v86, v86, v94
	v_add_f32_e32 v87, v87, v95
	v_add_f32_e32 v80, v80, v84
	v_add_f32_e32 v81, v81, v85
	v_add_f32_e32 v82, v82, v86
	v_add_f32_e32 v83, v83, v87
	v_add_f32_e32 v80, v80, v82
	v_add_f32_e32 v81, v81, v83
	v_add_f32_e32 v80, v80, v81
	v_add_f32_e32 v201, v201, v80
	s_add_i32 s5, s2, 0
	s_and_b32 s5, s5, 1
	s_mul_i32 s15, s5, 0x5000
	v_add_u32_e32 v191, s15, v196
	s_mul_i32 s15, s5, 0x4400
	s_add_i32 s16, s2, 2
	s_cmp_ge_u32 s16, 36
	s_cselect_b32 s15, 80000, s15
	v_add_u32_e32 v179, s15, v144
	s_xor_b32 s5, s5, 1
	s_mul_i32 s15, s5, 0x4400
	v_add_u32_e32 v190, s15, v197
	s_mul_i32 s15, s5, 0x5000
	s_add_i32 s16, s2, 1
	s_cmp_ge_u32 s16, 36
	s_cselect_b32 s15, 62592, s15
	v_add_u32_e32 v185, s15, v194
	s_barrier
	s_add_i32 s5, s2, 3
	s_cmp_ge_u32 s5, 36
	s_cbranch_scc1 .Latt_drain_0
	s_waitcnt vmcnt(4)
	s_branch .Latt_stage_0

; #define MFMA32(a, b, c) __builtin_amdgcn_mfma_f32_32x32x16_bf16((a), (b), (c), 0, 0, 0)
; __device__ __forceinline__ void attn_unit(const Frame& F, int layer, int qrow0, int ntiles, int b, int head, float lam, float m2, float lam_init) {
;     ...
;         bf16x8 vfa[4], vfb[4];
; #pragma unroll
;         for (int j = 0; j < 4; ++j) vfa[j] = frag_tr_acc(Vt, AT_VSTR, 0, 32 * j, lane);
; #pragma unroll
;         for (int ks = 0; ks < 4; ks += 2) {
; #pragma unroll
;             for (int j = 0; j < 4; ++j) vfb[j] = frag_tr_acc(Vt, AT_VSTR, 16 * (ks + 1), 32 * j, lane);
; #pragma unroll
;             for (int j = 0; j < 4; ++j) o[j] = MFMA32(pk[ks], vfa[j], o[j]);
;             __builtin_amdgcn_sched_barrier(0);
;             if (ks + 2 < 4) {
; #pragma unroll
;                 for (int j = 0; j < 4; ++j) vfa[j] = frag_tr_acc(Vt, AT_VSTR, 16 * (ks + 2), 32 * j, lane);
;             }
; #pragma unroll
;             for (int j = 0; j < 4; ++j) o[j] = MFMA32(pk[ks + 1], vfb[j], o[j]);
;             __builtin_amdgcn_sched_barrier(0);
;         }
.Latt_pv_0:
	v_mfma_f32_32x32x16_bf16 v[32:47], v[112:115], v[202:205], v[32:47]
	v_mfma_f32_32x32x16_bf16 v[48:63], v[112:115], v[206:209], v[48:63]
	v_mfma_f32_32x32x16_bf16 v[0:15], v[112:115], v[210:213], v[0:15]
	v_mfma_f32_32x32x16_bf16 v[16:31], v[112:115], v[214:217], v[16:31]
	ds_read_b64_tr_b16 v[202:203], v191 offset:45056
	ds_read_b64_tr_b16 v[206:207], v191 offset:45120
	ds_read_b64_tr_b16 v[210:211], v191 offset:45184
	ds_read_b64_tr_b16 v[214:215], v191 offset:45248
	ds_read_b64_tr_b16 v[204:205], v191 offset:47616
	ds_read_b64_tr_b16 v[208:209], v191 offset:47680
	ds_read_b64_tr_b16 v[212:213], v191 offset:47744
	s_waitcnt lgkmcnt(14)
	ds_read_b64_tr_b16 v[216:217], v191 offset:47808
	s_waitcnt lgkmcnt(8)
	v_mfma_f32_32x32x16_bf16 v[32:47], v[116:119], v[218:221], v[32:47]
	v_mfma_f32_32x32x16_bf16 v[48:63], v[116:119], v[222:225], v[48:63]
	v_mfma_f32_32x32x16_bf16 v[0:15], v[116:119], v[226:229], v[0:15]
	v_mfma_f32_32x32x16_bf16 v[16:31], v[116:119], v[230:233], v[16:31]
	ds_read_b64_tr_b16 v[218:219], v191 offset:50176
	ds_read_b64_tr_b16 v[222:223], v191 offset:50240
	ds_read_b64_tr_b16 v[226:227], v191 offset:50304
	ds_read_b64_tr_b16 v[230:231], v191 offset:50368
	ds_read_b64_tr_b16 v[220:221], v191 offset:52736
	ds_read_b64_tr_b16 v[224:225], v191 offset:52800
	ds_read_b64_tr_b16 v[228:229], v191 offset:52864
	s_waitcnt lgkmcnt(14)
	ds_read_b64_tr_b16 v[232:233], v191 offset:52928
	s_waitcnt lgkmcnt(8)
	v_mfma_f32_32x32x16_bf16 v[32:47], v[120:123], v[202:205], v[32:47]
	v_mfma_f32_32x32x16_bf16 v[48:63], v[120:123], v[206:209], v[48:63]
	v_mfma_f32_32x32x16_bf16 v[0:15], v[120:123], v[210:213], v[0:15]
	v_mfma_f32_32x32x16_bf16 v[16:31], v[120:123], v[214:217], v[16:31]
	s_waitcnt lgkmcnt(0)
	s_barrier
	s_add_i32 s5, s2, 4
	s_cmp_ge_u32 s5, 36
	s_cbranch_scc1 .Latt_nokload_it1
	s_cmp_lt_u32 s5, 4
	s_cselect_b32 s15, s42, s43
	s_lshl_b32 s45, s5, 6
	s_add_i32 s15, s15, s45
	s_lshl_b32 s15, s15, 10
	v_add_u32_e32 v186, s15, v178
	v_add_u32_e32 v187, 0x8000, v186
	global_load_dwordx4 v[162:165], v186, s[72:73]
	global_load_dwordx4 v[166:169], v187, s[72:73]

; #define LAS __attribute__((address_space(3)))
; __device__ __forceinline__ unsigned pk2(float lo, float hi) { f32x2_t v = {lo, hi}; bf16x2_t b = __builtin_convertvector(v, bf16x2_t); return __builtin_bit_cast(unsigned, b); }
; #define AT_STOREK(st) do { _Pragma("unroll") for (int i_ = 0; i_ < 2; ++i_) *(LAS u32x4*)(L + AT_K + (st) * AT_KBYTES + (prow0 + 32 * i_) * AT_KSTR + pch * 16) = kreg[i_]; } while (0)
; #define AT_STOREV(st) do { _Pragma("unroll") for (int i_ = 0; i_ < 2; ++i_) *(LAS u32x4*)(L + AT_V + (st) * AT_VBYTES + (prow0 + 32 * i_) * AT_VSTR + pch * 16) = vreg[i_]; } while (0)
; __device__ __forceinline__ void attn_unit(const Frame& F, int layer, int qrow0, int ntiles, int b, int head, float lam, float m2, float lam_init) {
;     ...
;         float ls = 0.f;
; #pragma unroll
;         for (int i = 0; i < 16; ++i) { sa[i] = __builtin_amdgcn_exp2f(sa[i]); sb[i] = __builtin_amdgcn_exp2f(sb[i]); ls += sa[i] + sb[i]; }
;         lsum += ls;
;         bf16x8 pk[4];
;         { u32x4 w0, w1, w2, w3;
; #pragma unroll
;           for (int i = 0; i < 4; ++i) { w0[i] = pk2(sa[2 * i], sa[2 * i + 1]); w1[i] = pk2(sa[8 + 2 * i], sa[9 + 2 * i]); w2[i] = pk2(sb[2 * i], sb[2 * i + 1]); w3[i] = pk2(sb[8 + 2 * i], sb[9 + 2 * i]); }
;           pk[0] = __builtin_bit_cast(bf16x8, w0); pk[1] = __builtin_bit_cast(bf16x8, w1); pk[2] = __builtin_bit_cast(bf16x8, w2); pk[3] = __builtin_bit_cast(bf16x8, w3); }
;         LAS const unsigned char* Vt = L + AT_V + (t & 1) * AT_VBYTES;
;     ...
;         if (t + 2 < ntiles) AT_STOREK(t & 1);
;         if (t + 1 < ntiles) AT_STOREV((t + 1) & 1);
;         __syncthreads();
;         sa = na; sb = nb;
.Latt_novload_it1:
	v_mfma_f32_32x32x16_bf16 v[32:47], v[124:127], v[218:221], v[32:47]
	v_mfma_f32_32x32x16_bf16 v[48:63], v[124:127], v[222:225], v[48:63]
	v_mfma_f32_32x32x16_bf16 v[0:15], v[124:127], v[226:229], v[0:15]
	v_mfma_f32_32x32x16_bf16 v[16:31], v[124:127], v[230:233], v[16:31]
	v_exp_f32_e32 v80, v80
	v_exp_f32_e32 v96, v96
	v_exp_f32_e32 v81, v81
	v_exp_f32_e32 v97, v97
	v_exp_f32_e32 v82, v82
	v_exp_f32_e32 v98, v98
	v_exp_f32_e32 v83, v83
	v_exp_f32_e32 v99, v99
	v_exp_f32_e32 v84, v84
	v_exp_f32_e32 v100, v100
	v_exp_f32_e32 v85, v85
	v_exp_f32_e32 v101, v101
	v_exp_f32_e32 v86, v86
	v_exp_f32_e32 v102, v102
	v_exp_f32_e32 v87, v87
	v_exp_f32_e32 v103, v103
	v_exp_f32_e32 v88, v88
	v_exp_f32_e32 v104, v104
	v_exp_f32_e32 v89, v89
	v_exp_f32_e32 v105, v105
	v_exp_f32_e32 v90, v90
	v_exp_f32_e32 v106, v106
	v_exp_f32_e32 v91, v91
	v_exp_f32_e32 v107, v107
	v_exp_f32_e32 v92, v92
	v_exp_f32_e32 v108, v108
	v_exp_f32_e32 v93, v93
	v_exp_f32_e32 v109, v109
	v_exp_f32_e32 v94, v94
	v_exp_f32_e32 v110, v110
	v_exp_f32_e32 v95, v95
	v_exp_f32_e32 v111, v111
	v_cvt_pk_bf16_f32 v112, v80, v81
	v_cvt_pk_bf16_f32 v113, v82, v83
	v_cvt_pk_bf16_f32 v114, v84, v85
	v_cvt_pk_bf16_f32 v115, v86, v87
	v_cvt_pk_bf16_f32 v116, v88, v89
	v_cvt_pk_bf16_f32 v117, v90, v91
	v_cvt_pk_bf16_f32 v118, v92, v93
	v_cvt_pk_bf16_f32 v119, v94, v95
	v_cvt_pk_bf16_f32 v120, v96, v97
	v_cvt_pk_bf16_f32 v121, v98, v99
	v_cvt_pk_bf16_f32 v122, v100, v101
	v_cvt_pk_bf16_f32 v123, v102, v103
	v_cvt_pk_bf16_f32 v180, v104, v105
	v_cvt_pk_bf16_f32 v181, v106, v107
	v_cvt_pk_bf16_f32 v182, v108, v109
	v_cvt_pk_bf16_f32 v183, v110, v111
	v_add_f32_e32 v80, v80, v96
	v_add_f32_e32 v81, v81, v97
	v_add_f32_e32 v82, v82, v98
	v_add_f32_e32 v83, v83, v99
	v_add_f32_e32 v84, v84, v100
	v_add_f32_e32 v85, v85, v101
	v_add_f32_e32 v86, v86, v102
	v_add_f32_e32 v87, v87, v103
	v_add_f32_e32 v88, v88, v104
	v_add_f32_e32 v89, v89, v105
	v_add_f32_e32 v90, v90, v106
	v_add_f32_e32 v91, v91, v107
	v_add_f32_e32 v92, v92, v108
	v_add_f32_e32 v93, v93, v109
	v_add_f32_e32 v94, v94, v110
	v_add_f32_e32 v95, v95, v111
	v_add_f32_e32 v80, v80, v88
	v_add_f32_e32 v81, v81, v89
	v_add_f32_e32 v82, v82, v90
	v_add_f32_e32 v83, v83, v91
	v_add_f32_e32 v84, v84, v92
	v_add_f32_e32 v85, v85, v93
	v_add_f32_e32 v86, v86, v94
	v_add_f32_e32 v87, v87, v95
	v_add_f32_e32 v80, v80, v84
	v_add_f32_e32 v81, v81, v85
	v_add_f32_e32 v82, v82, v86
	v_add_f32_e32 v83, v83, v87
	v_add_f32_e32 v80, v80, v82
	v_add_f32_e32 v81, v81, v83
	v_add_f32_e32 v80, v80, v81
	v_add_f32_e32 v201, v201, v80
	s_add_i32 s5, s2, 1
	s_and_b32 s5, s5, 1
	s_mul_i32 s15, s5, 0x5000
	v_add_u32_e32 v191, s15, v196
	s_mul_i32 s15, s5, 0x4400
	s_add_i32 s16, s2, 3
	s_cmp_ge_u32 s16, 36
	s_cselect_b32 s15, 80000, s15
	v_add_u32_e32 v179, s15, v144
	s_xor_b32 s5, s5, 1
	s_mul_i32 s15, s5, 0x4400
	v_add_u32_e32 v190, s15, v197
	s_mul_i32 s15, s5, 0x5000
	s_add_i32 s16, s2, 2
	s_cmp_ge_u32 s16, 36
	s_cselect_b32 s15, 62592, s15
	v_add_u32_e32 v185, s15, v194
	s_barrier
	s_add_i32 s5, s2, 4
	s_cmp_ge_u32 s5, 36
	s_cbranch_scc1 .Latt_drain_1
	s_waitcnt vmcnt(4)
	s_branch .Latt_stage_1

; #define MFMA32(a, b, c) __builtin_amdgcn_mfma_f32_32x32x16_bf16((a), (b), (c), 0, 0, 0)
; #define AT_STOREK(st) do { _Pragma("unroll") for (int i_ = 0; i_ < 2; ++i_) *(LAS u32x4*)(L + AT_K + (st) * AT_KBYTES + (prow0 + 32 * i_) * AT_KSTR + pch * 16) = kreg[i_]; } while (0)
; #define AT_STOREV(st) do { _Pragma("unroll") for (int i_ = 0; i_ < 2; ++i_) *(LAS u32x4*)(L + AT_V + (st) * AT_VBYTES + (prow0 + 32 * i_) * AT_VSTR + pch * 16) = vreg[i_]; } while (0)
; __device__ __forceinline__ void attn_unit(const Frame& F, int layer, int qrow0, int ntiles, int b, int head, float lam, float m2, float lam_init) {
;     ...
;         bf16x8 vfa[4], vfb[4];
; #pragma unroll
;         for (int j = 0; j < 4; ++j) vfa[j] = frag_tr_acc(Vt, AT_VSTR, 0, 32 * j, lane);
; #pragma unroll
;         for (int ks = 0; ks < 4; ks += 2) {
; #pragma unroll
;             for (int j = 0; j < 4; ++j) vfb[j] = frag_tr_acc(Vt, AT_VSTR, 16 * (ks + 1), 32 * j, lane);
; #pragma unroll
;             for (int j = 0; j < 4; ++j) o[j] = MFMA32(pk[ks], vfa[j], o[j]);
;             __builtin_amdgcn_sched_barrier(0);
;             if (ks + 2 < 4) {
; #pragma unroll
;                 for (int j = 0; j < 4; ++j) vfa[j] = frag_tr_acc(Vt, AT_VSTR, 16 * (ks + 2), 32 * j, lane);
;             }
; #pragma unroll
;             for (int j = 0; j < 4; ++j) o[j] = MFMA32(pk[ks + 1], vfb[j], o[j]);
;             __builtin_amdgcn_sched_barrier(0);
;         }
;         if (t + 2 < ntiles) AT_STOREK(t & 1);
;         if (t + 1 < ntiles) AT_STOREV((t + 1) & 1);
;         __syncthreads();
;         sa = na; sb = nb;
;     }
.Latt_pv_1:
	v_mfma_f32_32x32x16_bf16 v[32:47], v[112:115], v[202:205], v[32:47]
	v_mfma_f32_32x32x16_bf16 v[48:63], v[112:115], v[206:209], v[48:63]
	v_mfma_f32_32x32x16_bf16 v[0:15], v[112:115], v[210:213], v[0:15]
	v_mfma_f32_32x32x16_bf16 v[16:31], v[112:115], v[214:217], v[16:31]
	ds_read_b64_tr_b16 v[202:203], v191 offset:45056
	ds_read_b64_tr_b16 v[206:207], v191 offset:45120
	ds_read_b64_tr_b16 v[210:211], v191 offset:45184
	ds_read_b64_tr_b16 v[214:215], v191 offset:45248
	ds_read_b64_tr_b16 v[204:205], v191 offset:47616
	ds_read_b64_tr_b16 v[208:209], v191 offset:47680
	ds_read_b64_tr_b16 v[212:213], v191 offset:47744
	s_waitcnt lgkmcnt(14)
	ds_read_b64_tr_b16 v[216:217], v191 offset:47808
	s_waitcnt lgkmcnt(8)
	v_mfma_f32_32x32x16_bf16 v[32:47], v[116:119], v[218:221], v[32:47]
	v_mfma_f32_32x32x16_bf16 v[48:63], v[116:119], v[222:225], v[48:63]
	v_mfma_f32_32x32x16_bf16 v[0:15], v[116:119], v[226:229], v[0:15]
	v_mfma_f32_32x32x16_bf16 v[16:31], v[116:119], v[230:233], v[16:31]
	ds_read_b64_tr_b16 v[218:219], v191 offset:50176
	ds_read_b64_tr_b16 v[222:223], v191 offset:50240
	ds_read_b64_tr_b16 v[226:227], v191 offset:50304
	ds_read_b64_tr_b16 v[230:231], v191 offset:50368
	ds_read_b64_tr_b16 v[220:221], v191 offset:52736
	ds_read_b64_tr_b16 v[224:225], v191 offset:52800
	ds_read_b64_tr_b16 v[228:229], v191 offset:52864
	s_waitcnt lgkmcnt(14)
	ds_read_b64_tr_b16 v[232:233], v191 offset:52928
	s_waitcnt lgkmcnt(8)
	v_mfma_f32_32x32x16_bf16 v[32:47], v[120:123], v[202:205], v[32:47]
	v_mfma_f32_32x32x16_bf16 v[48:63], v[120:123], v[206:209], v[48:63]
	v_mfma_f32_32x32x16_bf16 v[0:15], v[120:123], v[210:213], v[0:15]
	v_mfma_f32_32x32x16_bf16 v[16:31], v[120:123], v[214:217], v[16:31]
	s_waitcnt lgkmcnt(0)
	s_barrier
	s_add_i32 s2, s2, 2
	s_cmp_lt_u32 s2, 36
	s_cbranch_scc1 .Latt_loop
	v_mfma_f32_32x32x16_bf16 v[32:47], v[180:183], v[218:221], v[32:47]
	v_mfma_f32_32x32x16_bf16 v[48:63], v[180:183], v[222:225], v[48:63]
	v_mfma_f32_32x32x16_bf16 v[0:15], v[180:183], v[226:229], v[0:15]
	v_mfma_f32_32x32x16_bf16 v[16:31], v[180:183], v[230:233], v[16:31]
	s_cmp_ge_u32 s12, 4
	s_cbranch_scc1 .Latt_trail1
	s_barrier
